# plus: GEMM LDS-DMA staging loads in saddr form where the address was scalar base + 32-bit lane offset (23 fewer 64-bit VALU adds per K-loop iteration set)
# baseline (speedup 1.0000x reference)
.LBB0_514:
	s_add_u32 s22, s82, s92
	s_addc_u32 s23, s83, s93
	s_add_u32 s24, s22, 0x100
	s_addc_u32 s25, s23, 0
	s_add_u32 s58, s3, s92
	s_addc_u32 s59, s2, s93
	s_add_i32 vcc_lo, 0, 0x10000
	s_cmpk_eq_i32 s92, 0xf00
	s_cselect_b64 s[26:27], -1, 0
	s_and_b64 s[22:23], s[26:27], exec
	s_cselect_b32 s25, s67, s25
	s_cselect_b32 s24, s75, s24
	s_cselect_b32 s23, s95, s59
	s_cselect_b32 s22, s29, s58
	s_add_i32 vcc_hi, 0, 0x14000
	v_add_u32_e32 v130, vcc_lo, v223
	v_add_u32_e32 v142, vcc_hi, v223
	ds_read_b128 v[146:149], v130
	ds_read_b128 v[150:153], v130 offset:1024
	ds_read_b128 v[154:157], v130 offset:2048
	ds_read_b128 v[158:161], v130 offset:3072
	ds_read_b128 v[130:133], v142
	ds_read_b128 v[134:137], v142 offset:1024
	ds_read_b128 v[138:141], v142 offset:2048
	ds_read_b128 v[142:145], v142 offset:3072
	v_lshl_add_u64 v[214:215], v[210:211], 0, s[92:93]
	s_add_i32 m0, s81, 0xc000
	s_waitcnt lgkmcnt(0)
	ds_read_b128 v[162:165], v224
	ds_read_b128 v[166:169], v224 offset:1024
	ds_read_b128 v[170:173], v224 offset:2048
	ds_read_b128 v[174:177], v224 offset:3072
	ds_read_b128 v[178:181], v224 offset:4096
	ds_read_b128 v[182:185], v224 offset:5120
	ds_read_b128 v[186:189], v224 offset:6144
	ds_read_b128 v[190:193], v224 offset:7168
	global_load_lds_dwordx4 v[214:215], off
	v_lshl_add_u64 v[214:215], v[212:213], 0, s[92:93]
	s_add_i32 m0, s81, 0xe000
	s_nop 0
	global_load_lds_dwordx4 v[214:215], off
	s_waitcnt vmcnt(8)
	s_waitcnt lgkmcnt(0)
	s_barrier
	v_mfma_f32_16x16x32_bf16 v[124:127], v[146:149], v[162:165], v[124:127]
	v_mfma_f32_16x16x32_bf16 v[120:123], v[154:157], v[162:165], v[120:123]
	v_mfma_f32_16x16x32_bf16 v[116:119], v[146:149], v[170:173], v[116:119]
	v_mfma_f32_16x16x32_bf16 v[108:111], v[154:157], v[170:173], v[108:111]
	v_mfma_f32_16x16x32_bf16 v[100:103], v[146:149], v[178:181], v[100:103]
	v_mfma_f32_16x16x32_bf16 v[92:95], v[154:157], v[178:181], v[92:95]
	v_mfma_f32_16x16x32_bf16 v[84:87], v[146:149], v[186:189], v[84:87]
	v_mfma_f32_16x16x32_bf16 v[76:79], v[154:157], v[186:189], v[76:79]
	v_mfma_f32_16x16x32_bf16 v[124:127], v[150:153], v[166:169], v[124:127]
	v_mfma_f32_16x16x32_bf16 v[120:123], v[158:161], v[166:169], v[120:123]
	v_mfma_f32_16x16x32_bf16 v[116:119], v[150:153], v[174:177], v[116:119]
	v_mfma_f32_16x16x32_bf16 v[108:111], v[158:161], v[174:177], v[108:111]
	v_mfma_f32_16x16x32_bf16 v[100:103], v[150:153], v[182:185], v[100:103]
	v_mfma_f32_16x16x32_bf16 v[92:95], v[158:161], v[182:185], v[92:95]
	v_mfma_f32_16x16x32_bf16 v[84:87], v[150:153], v[190:193], v[84:87]
	v_mfma_f32_16x16x32_bf16 v[76:79], v[158:161], v[190:193], v[76:79]
	v_mfma_f32_16x16x32_bf16 v[112:115], v[130:133], v[162:165], v[112:115]
	v_mfma_f32_16x16x32_bf16 v[104:107], v[138:141], v[162:165], v[104:107]
	v_mfma_f32_16x16x32_bf16 v[96:99], v[130:133], v[170:173], v[96:99]
	v_mfma_f32_16x16x32_bf16 v[88:91], v[138:141], v[170:173], v[88:91]
	v_mfma_f32_16x16x32_bf16 v[80:83], v[130:133], v[178:181], v[80:83]
	v_mfma_f32_16x16x32_bf16 v[72:75], v[138:141], v[178:181], v[72:75]
	v_mfma_f32_16x16x32_bf16 v[68:71], v[130:133], v[186:189], v[68:71]
	v_mfma_f32_16x16x32_bf16 v[64:67], v[138:141], v[186:189], v[64:67]
	v_mfma_f32_16x16x32_bf16 v[112:115], v[134:137], v[166:169], v[112:115]
	v_mfma_f32_16x16x32_bf16 v[104:107], v[142:145], v[166:169], v[104:107]
	v_mfma_f32_16x16x32_bf16 v[96:99], v[134:137], v[174:177], v[96:99]
	v_mfma_f32_16x16x32_bf16 v[88:91], v[142:145], v[174:177], v[88:91]
	v_mfma_f32_16x16x32_bf16 v[80:83], v[134:137], v[182:185], v[80:83]
	v_mfma_f32_16x16x32_bf16 v[72:75], v[142:145], v[182:185], v[72:75]
	v_mfma_f32_16x16x32_bf16 v[68:71], v[134:137], v[190:193], v[68:71]
	v_mfma_f32_16x16x32_bf16 v[64:67], v[142:145], v[190:193], v[64:67]
	s_barrier
	s_add_i32 s58, vcc_lo, s28
	v_lshl_add_u64 v[214:215], s[22:23], 0, v[200:201]
	s_mov_b32 m0, s58
	ds_read_b128 v[186:189], v224 offset:16384
	ds_read_b128 v[190:193], v224 offset:17408
	ds_read_b128 v[178:181], v224 offset:18432
	ds_read_b128 v[182:185], v224 offset:19456
	ds_read_b128 v[170:173], v224 offset:20480
	ds_read_b128 v[174:177], v224 offset:21504
	ds_read_b128 v[162:165], v224 offset:22528
	ds_read_b128 v[166:169], v224 offset:23552
	global_load_lds_dwordx4 v[214:215], off
	s_add_i32 m0, s58, 0x2000
	s_add_u32 s58, s22, 0x80000
	v_lshl_add_u64 v[216:217], s[22:23], 0, v[204:205]
	s_addc_u32 s59, s23, 0
	s_add_i32 vcc_lo, vcc_hi, s28
	global_load_lds_dwordx4 v[216:217], off
	s_mov_b32 m0, vcc_lo
	v_lshl_add_u64 v[220:221], s[24:25], 0, v[202:203]
	global_load_lds_dwordx4 v200, s[58:59]
	s_add_i32 m0, vcc_lo, 0x2000
	v_cndmask_b32_e64 v194, 0, 1, s[96:97]
	global_load_lds_dwordx4 v204, s[58:59]
	v_lshl_add_u64 v[218:219], s[24:25], 0, v[198:199]
	s_mov_b32 m0, s81
	v_cmp_ne_u32_e64 s[58:59], 1, v194
	global_load_lds_dwordx4 v[218:219], off
	s_mov_b32 m0, s88
	s_andn2_b64 vcc, exec, s[96:97]
	global_load_lds_dwordx4 v[220:221], off
	s_waitcnt vmcnt(8)
	s_waitcnt lgkmcnt(0)
	s_barrier
	s_cbranch_vccnz .LBB0_516
	s_waitcnt lgkmcnt(0)
	v_mfma_f32_16x16x32_bf16 v[60:63], v[146:149], v[186:189], v[60:63]
	v_mfma_f32_16x16x32_bf16 v[56:59], v[154:157], v[186:189], v[56:59]
	v_mfma_f32_16x16x32_bf16 v[44:47], v[146:149], v[178:181], v[44:47]
	v_mfma_f32_16x16x32_bf16 v[40:43], v[154:157], v[178:181], v[40:43]
	v_mfma_f32_16x16x32_bf16 v[28:31], v[146:149], v[170:173], v[28:31]
	v_mfma_f32_16x16x32_bf16 v[24:27], v[154:157], v[170:173], v[24:27]
	v_mfma_f32_16x16x32_bf16 v[12:15], v[146:149], v[162:165], v[12:15]
	v_mfma_f32_16x16x32_bf16 v[8:11], v[154:157], v[162:165], v[8:11]
	v_mfma_f32_16x16x32_bf16 v[60:63], v[150:153], v[190:193], v[60:63]
	v_mfma_f32_16x16x32_bf16 v[56:59], v[158:161], v[190:193], v[56:59]
	v_mfma_f32_16x16x32_bf16 v[44:47], v[150:153], v[182:185], v[44:47]
	v_mfma_f32_16x16x32_bf16 v[40:43], v[158:161], v[182:185], v[40:43]
	v_mfma_f32_16x16x32_bf16 v[28:31], v[150:153], v[174:177], v[28:31]
	v_mfma_f32_16x16x32_bf16 v[24:27], v[158:161], v[174:177], v[24:27]
	v_mfma_f32_16x16x32_bf16 v[12:15], v[150:153], v[166:169], v[12:15]
	v_mfma_f32_16x16x32_bf16 v[8:11], v[158:161], v[166:169], v[8:11]
	v_mfma_f32_16x16x32_bf16 v[52:55], v[130:133], v[186:189], v[52:55]
	v_mfma_f32_16x16x32_bf16 v[48:51], v[138:141], v[186:189], v[48:51]
	v_mfma_f32_16x16x32_bf16 v[36:39], v[130:133], v[178:181], v[36:39]
	v_mfma_f32_16x16x32_bf16 v[32:35], v[138:141], v[178:181], v[32:35]
	v_mfma_f32_16x16x32_bf16 v[20:23], v[130:133], v[170:173], v[20:23]
	v_mfma_f32_16x16x32_bf16 v[16:19], v[138:141], v[170:173], v[16:19]
	v_mfma_f32_16x16x32_bf16 v[4:7], v[130:133], v[162:165], v[4:7]
	v_mfma_f32_16x16x32_bf16 v[0:3], v[138:141], v[162:165], v[0:3]
	v_mfma_f32_16x16x32_bf16 v[52:55], v[134:137], v[190:193], v[52:55]
	v_mfma_f32_16x16x32_bf16 v[48:51], v[142:145], v[190:193], v[48:51]
	v_mfma_f32_16x16x32_bf16 v[36:39], v[134:137], v[182:185], v[36:39]
	v_mfma_f32_16x16x32_bf16 v[32:35], v[142:145], v[182:185], v[32:35]
	v_mfma_f32_16x16x32_bf16 v[20:23], v[134:137], v[174:177], v[20:23]
	v_mfma_f32_16x16x32_bf16 v[16:19], v[142:145], v[174:177], v[16:19]
	v_mfma_f32_16x16x32_bf16 v[4:7], v[134:137], v[166:169], v[4:7]
	v_mfma_f32_16x16x32_bf16 v[0:3], v[142:145], v[166:169], v[0:3]
.LBB0_516:
	s_barrier
	s_add_i32 vcc_lo, 0, 0x18000
	s_add_i32 vcc_hi, 0, 0x1c000
	v_add_u32_e32 v130, vcc_lo, v223
	v_add_u32_e32 v142, vcc_hi, v223
	ds_read_b128 v[146:149], v130
	ds_read_b128 v[150:153], v130 offset:1024
	ds_read_b128 v[154:157], v130 offset:2048
	ds_read_b128 v[158:161], v130 offset:3072
	ds_read_b128 v[130:133], v142
	ds_read_b128 v[134:137], v142 offset:1024
	ds_read_b128 v[138:141], v142 offset:2048
	ds_read_b128 v[142:145], v142 offset:3072
	s_and_b64 s[26:27], s[26:27], exec
	s_cselect_b32 s27, s72, s86
	s_cselect_b32 s26, 0, s87
	s_add_u32 s24, s24, s27
	s_addc_u32 s25, s25, s26
	s_mov_b32 m0, s89
	s_waitcnt lgkmcnt(0)
	ds_read_b128 v[162:165], v224 offset:32768
	ds_read_b128 v[166:169], v224 offset:33792
	ds_read_b128 v[170:173], v224 offset:34816
	ds_read_b128 v[174:177], v224 offset:35840
	ds_read_b128 v[178:181], v224 offset:36864
	ds_read_b128 v[182:185], v224 offset:37888
	ds_read_b128 v[186:189], v224 offset:38912
	ds_read_b128 v[190:193], v224 offset:39936
	global_load_lds_dwordx4 v198, s[24:25]
	s_mov_b32 m0, s90
	s_nop 0
	global_load_lds_dwordx4 v202, s[24:25]
	s_waitcnt vmcnt(8)
	s_waitcnt lgkmcnt(0)
	s_barrier
	v_mfma_f32_16x16x32_bf16 v[124:127], v[146:149], v[162:165], v[124:127]
	v_mfma_f32_16x16x32_bf16 v[120:123], v[154:157], v[162:165], v[120:123]
	v_mfma_f32_16x16x32_bf16 v[116:119], v[146:149], v[170:173], v[116:119]
	v_mfma_f32_16x16x32_bf16 v[108:111], v[154:157], v[170:173], v[108:111]
	v_mfma_f32_16x16x32_bf16 v[100:103], v[146:149], v[178:181], v[100:103]
	v_mfma_f32_16x16x32_bf16 v[92:95], v[154:157], v[178:181], v[92:95]
	v_mfma_f32_16x16x32_bf16 v[84:87], v[146:149], v[186:189], v[84:87]
	v_mfma_f32_16x16x32_bf16 v[76:79], v[154:157], v[186:189], v[76:79]
	v_mfma_f32_16x16x32_bf16 v[124:127], v[150:153], v[166:169], v[124:127]
	v_mfma_f32_16x16x32_bf16 v[120:123], v[158:161], v[166:169], v[120:123]
	v_mfma_f32_16x16x32_bf16 v[116:119], v[150:153], v[174:177], v[116:119]
	v_mfma_f32_16x16x32_bf16 v[108:111], v[158:161], v[174:177], v[108:111]
	v_mfma_f32_16x16x32_bf16 v[100:103], v[150:153], v[182:185], v[100:103]
	v_mfma_f32_16x16x32_bf16 v[92:95], v[158:161], v[182:185], v[92:95]
	v_mfma_f32_16x16x32_bf16 v[84:87], v[150:153], v[190:193], v[84:87]
	v_mfma_f32_16x16x32_bf16 v[76:79], v[158:161], v[190:193], v[76:79]
	v_mfma_f32_16x16x32_bf16 v[112:115], v[130:133], v[162:165], v[112:115]
	v_mfma_f32_16x16x32_bf16 v[104:107], v[138:141], v[162:165], v[104:107]
	v_mfma_f32_16x16x32_bf16 v[96:99], v[130:133], v[170:173], v[96:99]
	v_mfma_f32_16x16x32_bf16 v[88:91], v[138:141], v[170:173], v[88:91]
	v_mfma_f32_16x16x32_bf16 v[80:83], v[130:133], v[178:181], v[80:83]
	v_mfma_f32_16x16x32_bf16 v[72:75], v[138:141], v[178:181], v[72:75]
	v_mfma_f32_16x16x32_bf16 v[68:71], v[130:133], v[186:189], v[68:71]
	v_mfma_f32_16x16x32_bf16 v[64:67], v[138:141], v[186:189], v[64:67]
	v_mfma_f32_16x16x32_bf16 v[112:115], v[134:137], v[166:169], v[112:115]
	v_mfma_f32_16x16x32_bf16 v[104:107], v[142:145], v[166:169], v[104:107]
	v_mfma_f32_16x16x32_bf16 v[96:99], v[134:137], v[174:177], v[96:99]
	v_mfma_f32_16x16x32_bf16 v[88:91], v[142:145], v[174:177], v[88:91]
	v_mfma_f32_16x16x32_bf16 v[80:83], v[134:137], v[182:185], v[80:83]
	v_mfma_f32_16x16x32_bf16 v[72:75], v[142:145], v[182:185], v[72:75]
	v_mfma_f32_16x16x32_bf16 v[68:71], v[134:137], v[190:193], v[68:71]
	v_mfma_f32_16x16x32_bf16 v[64:67], v[142:145], v[190:193], v[64:67]
	s_barrier
	s_add_i32 s24, vcc_lo, s28
	v_lshl_add_u64 v[214:215], v[214:215], 0, s[42:43]
	s_mov_b32 m0, s24
	ds_read_b128 v[186:189], v224 offset:49152
	ds_read_b128 v[190:193], v224 offset:50176
	ds_read_b128 v[178:181], v224 offset:51200
	ds_read_b128 v[182:185], v224 offset:52224
	ds_read_b128 v[170:173], v224 offset:53248
	ds_read_b128 v[174:177], v224 offset:54272
	ds_read_b128 v[162:165], v224 offset:55296
	ds_read_b128 v[166:169], v224 offset:56320
	global_load_lds_dwordx4 v[214:215], off
	s_add_i32 m0, s24, 0x2000
	s_add_u32 s22, s22, 0x80080
	v_lshl_add_u64 v[214:215], v[216:217], 0, s[42:43]
	s_addc_u32 s23, s23, 0
	s_add_i32 s24, vcc_hi, s28
	global_load_lds_dwordx4 v[214:215], off
	s_mov_b32 m0, s24
	s_and_b64 vcc, exec, s[58:59]
	global_load_lds_dwordx4 v200, s[22:23]
	s_add_i32 m0, s24, 0x2000
	s_nop 0
	global_load_lds_dwordx4 v204, s[22:23]
	v_lshl_add_u64 v[214:215], v[218:219], 0, s[42:43]
	s_mov_b32 m0, s91
	s_nop 0
	global_load_lds_dwordx4 v[214:215], off
	v_lshl_add_u64 v[214:215], v[220:221], 0, s[42:43]
	s_mov_b32 m0, s94
	s_nop 0
	global_load_lds_dwordx4 v[214:215], off
	s_waitcnt vmcnt(8)
	s_waitcnt lgkmcnt(0)
	s_barrier
	s_cbranch_vccnz .LBB0_513
	s_waitcnt lgkmcnt(0)
	v_mfma_f32_16x16x32_bf16 v[60:63], v[146:149], v[186:189], v[60:63]
	v_mfma_f32_16x16x32_bf16 v[56:59], v[154:157], v[186:189], v[56:59]
	v_mfma_f32_16x16x32_bf16 v[44:47], v[146:149], v[178:181], v[44:47]
	v_mfma_f32_16x16x32_bf16 v[40:43], v[154:157], v[178:181], v[40:43]
	v_mfma_f32_16x16x32_bf16 v[28:31], v[146:149], v[170:173], v[28:31]
	v_mfma_f32_16x16x32_bf16 v[24:27], v[154:157], v[170:173], v[24:27]
	v_mfma_f32_16x16x32_bf16 v[12:15], v[146:149], v[162:165], v[12:15]
	v_mfma_f32_16x16x32_bf16 v[8:11], v[154:157], v[162:165], v[8:11]
	v_mfma_f32_16x16x32_bf16 v[60:63], v[150:153], v[190:193], v[60:63]
	v_mfma_f32_16x16x32_bf16 v[56:59], v[158:161], v[190:193], v[56:59]
	v_mfma_f32_16x16x32_bf16 v[44:47], v[150:153], v[182:185], v[44:47]
	v_mfma_f32_16x16x32_bf16 v[40:43], v[158:161], v[182:185], v[40:43]
	v_mfma_f32_16x16x32_bf16 v[28:31], v[150:153], v[174:177], v[28:31]
	v_mfma_f32_16x16x32_bf16 v[24:27], v[158:161], v[174:177], v[24:27]
	v_mfma_f32_16x16x32_bf16 v[12:15], v[150:153], v[166:169], v[12:15]
	v_mfma_f32_16x16x32_bf16 v[8:11], v[158:161], v[166:169], v[8:11]
	v_mfma_f32_16x16x32_bf16 v[52:55], v[130:133], v[186:189], v[52:55]
	v_mfma_f32_16x16x32_bf16 v[48:51], v[138:141], v[186:189], v[48:51]
	v_mfma_f32_16x16x32_bf16 v[36:39], v[130:133], v[178:181], v[36:39]
	v_mfma_f32_16x16x32_bf16 v[32:35], v[138:141], v[178:181], v[32:35]
	v_mfma_f32_16x16x32_bf16 v[20:23], v[130:133], v[170:173], v[20:23]
	v_mfma_f32_16x16x32_bf16 v[16:19], v[138:141], v[170:173], v[16:19]
	v_mfma_f32_16x16x32_bf16 v[4:7], v[130:133], v[162:165], v[4:7]
	v_mfma_f32_16x16x32_bf16 v[0:3], v[138:141], v[162:165], v[0:3]
	v_mfma_f32_16x16x32_bf16 v[52:55], v[134:137], v[190:193], v[52:55]
	v_mfma_f32_16x16x32_bf16 v[48:51], v[142:145], v[190:193], v[48:51]
	v_mfma_f32_16x16x32_bf16 v[36:39], v[134:137], v[182:185], v[36:39]
	v_mfma_f32_16x16x32_bf16 v[32:35], v[142:145], v[182:185], v[32:35]
	v_mfma_f32_16x16x32_bf16 v[20:23], v[134:137], v[174:177], v[20:23]
	v_mfma_f32_16x16x32_bf16 v[16:19], v[142:145], v[174:177], v[16:19]
	v_mfma_f32_16x16x32_bf16 v[4:7], v[134:137], v[166:169], v[4:7]
	v_mfma_f32_16x16x32_bf16 v[0:3], v[142:145], v[166:169], v[0:3]
	s_branch .LBB0_513

.LBB0_725:
	s_add_u32 s2, s64, 0xfffe0080
	s_addc_u32 s3, s65, -1
	s_add_i32 s29, 0, 0x10000
	s_cmp_eq_u32 s66, 4
	s_cselect_b32 s25, s61, s3
	s_cselect_b32 s24, s60, s2
	v_add_u32_e32 v145, s29, v143
	s_cselect_b32 s23, s63, s17
	s_cselect_b32 s22, s62, s15
	s_add_i32 s30, 0, 0x14000
	ds_read_b128 v[146:149], v145
	ds_read_b128 v[150:153], v145 offset:1024
	ds_read_b128 v[154:157], v145 offset:2048
	ds_read_b128 v[158:161], v145 offset:3072
	v_add_u32_e32 v145, s30, v143
	ds_read_b128 v[162:165], v145
	ds_read_b128 v[166:169], v145 offset:1024
	ds_read_b128 v[170:173], v145 offset:2048
	ds_read_b128 v[174:177], v145 offset:3072
	s_add_i32 m0, s53, 0xc000
	ds_read_b128 v[178:181], v144
	ds_read_b128 v[182:185], v144 offset:1024
	ds_read_b128 v[186:189], v144 offset:2048
	ds_read_b128 v[190:193], v144 offset:3072
	ds_read_b128 v[198:201], v144 offset:4096
	ds_read_b128 v[202:205], v144 offset:5120
	ds_read_b128 v[206:209], v144 offset:6144
	ds_read_b128 v[210:213], v144 offset:7168
	global_load_lds_dwordx4 v138, s[64:65]
	s_add_i32 m0, s53, 0xe000
	s_nop 0
	global_load_lds_dwordx4 v140, s[64:65]
	s_waitcnt vmcnt(8)
	s_waitcnt lgkmcnt(0)
	s_barrier
	v_mfma_f32_16x16x32_bf16 v[124:127], v[146:149], v[178:181], v[124:127]
	v_mfma_f32_16x16x32_bf16 v[120:123], v[154:157], v[178:181], v[120:123]
	v_mfma_f32_16x16x32_bf16 v[116:119], v[146:149], v[186:189], v[116:119]
	v_mfma_f32_16x16x32_bf16 v[108:111], v[154:157], v[186:189], v[108:111]
	v_mfma_f32_16x16x32_bf16 v[100:103], v[146:149], v[198:201], v[100:103]
	v_mfma_f32_16x16x32_bf16 v[92:95], v[154:157], v[198:201], v[92:95]
	v_mfma_f32_16x16x32_bf16 v[84:87], v[146:149], v[206:209], v[84:87]
	v_mfma_f32_16x16x32_bf16 v[76:79], v[154:157], v[206:209], v[76:79]
	v_mfma_f32_16x16x32_bf16 v[124:127], v[150:153], v[182:185], v[124:127]
	v_mfma_f32_16x16x32_bf16 v[120:123], v[158:161], v[182:185], v[120:123]
	v_mfma_f32_16x16x32_bf16 v[116:119], v[150:153], v[190:193], v[116:119]
	v_mfma_f32_16x16x32_bf16 v[108:111], v[158:161], v[190:193], v[108:111]
	v_mfma_f32_16x16x32_bf16 v[100:103], v[150:153], v[202:205], v[100:103]
	v_mfma_f32_16x16x32_bf16 v[92:95], v[158:161], v[202:205], v[92:95]
	v_mfma_f32_16x16x32_bf16 v[84:87], v[150:153], v[210:213], v[84:87]
	v_mfma_f32_16x16x32_bf16 v[76:79], v[158:161], v[210:213], v[76:79]
	v_mfma_f32_16x16x32_bf16 v[112:115], v[162:165], v[178:181], v[112:115]
	v_mfma_f32_16x16x32_bf16 v[104:107], v[170:173], v[178:181], v[104:107]
	v_mfma_f32_16x16x32_bf16 v[96:99], v[162:165], v[186:189], v[96:99]
	v_mfma_f32_16x16x32_bf16 v[88:91], v[170:173], v[186:189], v[88:91]
	v_mfma_f32_16x16x32_bf16 v[80:83], v[162:165], v[198:201], v[80:83]
	v_mfma_f32_16x16x32_bf16 v[72:75], v[170:173], v[198:201], v[72:75]
	v_mfma_f32_16x16x32_bf16 v[68:71], v[162:165], v[206:209], v[68:71]
	v_mfma_f32_16x16x32_bf16 v[64:67], v[170:173], v[206:209], v[64:67]
	v_mfma_f32_16x16x32_bf16 v[112:115], v[166:169], v[182:185], v[112:115]
	v_mfma_f32_16x16x32_bf16 v[104:107], v[174:177], v[182:185], v[104:107]
	v_mfma_f32_16x16x32_bf16 v[96:99], v[166:169], v[190:193], v[96:99]
	v_mfma_f32_16x16x32_bf16 v[88:91], v[174:177], v[190:193], v[88:91]
	v_mfma_f32_16x16x32_bf16 v[80:83], v[166:169], v[202:205], v[80:83]
	v_mfma_f32_16x16x32_bf16 v[72:75], v[174:177], v[202:205], v[72:75]
	v_mfma_f32_16x16x32_bf16 v[68:71], v[166:169], v[210:213], v[68:71]
	v_mfma_f32_16x16x32_bf16 v[64:67], v[174:177], v[210:213], v[64:67]
	s_barrier
	s_add_i32 s2, s29, s39
	v_lshl_add_u64 v[214:215], s[22:23], 0, v[134:135]
	s_mov_b32 m0, s2
	ds_read_b128 v[178:181], v144 offset:16384
	ds_read_b128 v[182:185], v144 offset:17408
	ds_read_b128 v[186:189], v144 offset:18432
	ds_read_b128 v[190:193], v144 offset:19456
	ds_read_b128 v[198:201], v144 offset:20480
	ds_read_b128 v[202:205], v144 offset:21504
	ds_read_b128 v[206:209], v144 offset:22528
	ds_read_b128 v[210:213], v144 offset:23552
	global_load_lds_dwordx4 v[214:215], off
	s_add_i32 m0, s2, 0x2000
	s_add_u32 s2, s22, 0x20000
	v_lshl_add_u64 v[216:217], s[22:23], 0, v[130:131]
	s_addc_u32 s3, s23, 0
	s_add_i32 s29, s30, s39
	global_load_lds_dwordx4 v[216:217], off
	s_mov_b32 m0, s29
	v_lshl_add_u64 v[220:221], s[24:25], 0, v[132:133]
	global_load_lds_dwordx4 v134, s[2:3]
	s_add_i32 m0, s29, 0x2000
	s_nop 0
	global_load_lds_dwordx4 v130, s[2:3]
	v_lshl_add_u64 v[218:219], s[24:25], 0, v[136:137]
	s_mov_b32 m0, s53
	s_nop 0
	global_load_lds_dwordx4 v[218:219], off
	s_mov_b32 m0, s68
	s_nop 0
	global_load_lds_dwordx4 v[220:221], off
	s_waitcnt vmcnt(8)
	s_waitcnt lgkmcnt(0)
	s_barrier
	v_mfma_f32_16x16x32_bf16 v[60:63], v[146:149], v[178:181], v[60:63]
	v_mfma_f32_16x16x32_bf16 v[56:59], v[154:157], v[178:181], v[56:59]
	v_mfma_f32_16x16x32_bf16 v[52:55], v[146:149], v[186:189], v[52:55]
	v_mfma_f32_16x16x32_bf16 v[44:47], v[154:157], v[186:189], v[44:47]
	v_mfma_f32_16x16x32_bf16 v[36:39], v[146:149], v[198:201], v[36:39]
	v_mfma_f32_16x16x32_bf16 v[28:31], v[154:157], v[198:201], v[28:31]
	v_mfma_f32_16x16x32_bf16 v[20:23], v[146:149], v[206:209], v[20:23]
	v_mfma_f32_16x16x32_bf16 v[12:15], v[154:157], v[206:209], v[12:15]
	v_mfma_f32_16x16x32_bf16 v[60:63], v[150:153], v[182:185], v[60:63]
	v_mfma_f32_16x16x32_bf16 v[56:59], v[158:161], v[182:185], v[56:59]
	v_mfma_f32_16x16x32_bf16 v[52:55], v[150:153], v[190:193], v[52:55]
	v_mfma_f32_16x16x32_bf16 v[44:47], v[158:161], v[190:193], v[44:47]
	v_mfma_f32_16x16x32_bf16 v[36:39], v[150:153], v[202:205], v[36:39]
	v_mfma_f32_16x16x32_bf16 v[28:31], v[158:161], v[202:205], v[28:31]
	v_mfma_f32_16x16x32_bf16 v[20:23], v[150:153], v[210:213], v[20:23]
	v_mfma_f32_16x16x32_bf16 v[12:15], v[158:161], v[210:213], v[12:15]
	v_mfma_f32_16x16x32_bf16 v[48:51], v[162:165], v[178:181], v[48:51]
	v_mfma_f32_16x16x32_bf16 v[40:43], v[170:173], v[178:181], v[40:43]
	v_mfma_f32_16x16x32_bf16 v[32:35], v[162:165], v[186:189], v[32:35]
	v_mfma_f32_16x16x32_bf16 v[24:27], v[170:173], v[186:189], v[24:27]
	v_mfma_f32_16x16x32_bf16 v[16:19], v[162:165], v[198:201], v[16:19]
	v_mfma_f32_16x16x32_bf16 v[8:11], v[170:173], v[198:201], v[8:11]
	v_mfma_f32_16x16x32_bf16 v[4:7], v[162:165], v[206:209], v[4:7]
	v_mfma_f32_16x16x32_bf16 v[0:3], v[170:173], v[206:209], v[0:3]
	v_mfma_f32_16x16x32_bf16 v[48:51], v[166:169], v[182:185], v[48:51]
	v_mfma_f32_16x16x32_bf16 v[40:43], v[174:177], v[182:185], v[40:43]
	v_mfma_f32_16x16x32_bf16 v[32:35], v[166:169], v[190:193], v[32:35]
	v_mfma_f32_16x16x32_bf16 v[24:27], v[174:177], v[190:193], v[24:27]
	v_mfma_f32_16x16x32_bf16 v[16:19], v[166:169], v[202:205], v[16:19]
	v_mfma_f32_16x16x32_bf16 v[8:11], v[174:177], v[202:205], v[8:11]
	v_mfma_f32_16x16x32_bf16 v[4:7], v[166:169], v[210:213], v[4:7]
	v_mfma_f32_16x16x32_bf16 v[0:3], v[174:177], v[210:213], v[0:3]
	s_barrier
	s_add_i32 s29, 0, 0x18000
	v_add_u32_e32 v145, s29, v143
	s_add_i32 s30, 0, 0x1c000
	ds_read_b128 v[146:149], v145
	ds_read_b128 v[150:153], v145 offset:1024
	ds_read_b128 v[154:157], v145 offset:2048
	ds_read_b128 v[158:161], v145 offset:3072
	v_add_u32_e32 v145, s30, v143
	ds_read_b128 v[162:165], v145
	ds_read_b128 v[166:169], v145 offset:1024
	ds_read_b128 v[170:173], v145 offset:2048
	ds_read_b128 v[174:177], v145 offset:3072
	s_add_u32 s2, s24, 0x20000
	s_addc_u32 s3, s25, 0
	s_mov_b32 m0, s69
	ds_read_b128 v[178:181], v144 offset:32768
	ds_read_b128 v[182:185], v144 offset:33792
	ds_read_b128 v[186:189], v144 offset:34816
	ds_read_b128 v[190:193], v144 offset:35840
	ds_read_b128 v[198:201], v144 offset:36864
	ds_read_b128 v[202:205], v144 offset:37888
	ds_read_b128 v[206:209], v144 offset:38912
	ds_read_b128 v[210:213], v144 offset:39936
	global_load_lds_dwordx4 v136, s[2:3]
	s_mov_b32 m0, s70
	s_nop 0
	global_load_lds_dwordx4 v132, s[2:3]
	s_waitcnt vmcnt(8)
	s_waitcnt lgkmcnt(0)
	s_barrier
	v_mfma_f32_16x16x32_bf16 v[124:127], v[146:149], v[178:181], v[124:127]
	v_mfma_f32_16x16x32_bf16 v[120:123], v[154:157], v[178:181], v[120:123]
	v_mfma_f32_16x16x32_bf16 v[116:119], v[146:149], v[186:189], v[116:119]
	v_mfma_f32_16x16x32_bf16 v[108:111], v[154:157], v[186:189], v[108:111]
	v_mfma_f32_16x16x32_bf16 v[100:103], v[146:149], v[198:201], v[100:103]
	v_mfma_f32_16x16x32_bf16 v[92:95], v[154:157], v[198:201], v[92:95]
	v_mfma_f32_16x16x32_bf16 v[84:87], v[146:149], v[206:209], v[84:87]
	v_mfma_f32_16x16x32_bf16 v[76:79], v[154:157], v[206:209], v[76:79]
	v_mfma_f32_16x16x32_bf16 v[124:127], v[150:153], v[182:185], v[124:127]
	v_mfma_f32_16x16x32_bf16 v[120:123], v[158:161], v[182:185], v[120:123]
	v_mfma_f32_16x16x32_bf16 v[116:119], v[150:153], v[190:193], v[116:119]
	v_mfma_f32_16x16x32_bf16 v[108:111], v[158:161], v[190:193], v[108:111]
	v_mfma_f32_16x16x32_bf16 v[100:103], v[150:153], v[202:205], v[100:103]
	v_mfma_f32_16x16x32_bf16 v[92:95], v[158:161], v[202:205], v[92:95]
	v_mfma_f32_16x16x32_bf16 v[84:87], v[150:153], v[210:213], v[84:87]
	v_mfma_f32_16x16x32_bf16 v[76:79], v[158:161], v[210:213], v[76:79]
	v_mfma_f32_16x16x32_bf16 v[112:115], v[162:165], v[178:181], v[112:115]
	v_mfma_f32_16x16x32_bf16 v[104:107], v[170:173], v[178:181], v[104:107]
	v_mfma_f32_16x16x32_bf16 v[96:99], v[162:165], v[186:189], v[96:99]
	v_mfma_f32_16x16x32_bf16 v[88:91], v[170:173], v[186:189], v[88:91]
	v_mfma_f32_16x16x32_bf16 v[80:83], v[162:165], v[198:201], v[80:83]
	v_mfma_f32_16x16x32_bf16 v[72:75], v[170:173], v[198:201], v[72:75]
	v_mfma_f32_16x16x32_bf16 v[68:71], v[162:165], v[206:209], v[68:71]
	v_mfma_f32_16x16x32_bf16 v[64:67], v[170:173], v[206:209], v[64:67]
	v_mfma_f32_16x16x32_bf16 v[112:115], v[166:169], v[182:185], v[112:115]
	v_mfma_f32_16x16x32_bf16 v[104:107], v[174:177], v[182:185], v[104:107]
	v_mfma_f32_16x16x32_bf16 v[96:99], v[166:169], v[190:193], v[96:99]
	v_mfma_f32_16x16x32_bf16 v[88:91], v[174:177], v[190:193], v[88:91]
	v_mfma_f32_16x16x32_bf16 v[80:83], v[166:169], v[202:205], v[80:83]
	v_mfma_f32_16x16x32_bf16 v[72:75], v[174:177], v[202:205], v[72:75]
	v_mfma_f32_16x16x32_bf16 v[68:71], v[166:169], v[210:213], v[68:71]
	v_mfma_f32_16x16x32_bf16 v[64:67], v[174:177], v[210:213], v[64:67]
	s_barrier
	s_add_i32 s2, s29, s39
	v_lshl_add_u64 v[214:215], v[214:215], 0, s[42:43]
	s_mov_b32 m0, s2
	ds_read_b128 v[178:181], v144 offset:49152
	ds_read_b128 v[182:185], v144 offset:50176
	ds_read_b128 v[186:189], v144 offset:51200
	ds_read_b128 v[190:193], v144 offset:52224
	ds_read_b128 v[198:201], v144 offset:53248
	ds_read_b128 v[202:205], v144 offset:54272
	ds_read_b128 v[206:209], v144 offset:55296
	ds_read_b128 v[210:213], v144 offset:56320
	global_load_lds_dwordx4 v[214:215], off
	s_add_i32 m0, s2, 0x2000
	s_add_u32 s2, s22, 0x20080
	v_lshl_add_u64 v[214:215], v[216:217], 0, s[42:43]
	s_addc_u32 s3, s23, 0
	s_add_i32 s22, s30, s39
	global_load_lds_dwordx4 v[214:215], off
	s_mov_b32 m0, s22
	s_nop 0
	global_load_lds_dwordx4 v134, s[2:3]
	s_add_i32 m0, s22, 0x2000
	s_nop 0
	global_load_lds_dwordx4 v130, s[2:3]
	v_lshl_add_u64 v[214:215], v[218:219], 0, s[42:43]
	s_mov_b32 m0, s71
	s_nop 0
	global_load_lds_dwordx4 v[214:215], off
	v_lshl_add_u64 v[214:215], v[220:221], 0, s[42:43]
	s_mov_b32 m0, s74
	s_nop 0
	global_load_lds_dwordx4 v[214:215], off
	s_waitcnt vmcnt(8)
	s_waitcnt lgkmcnt(0)
	s_barrier
	v_mfma_f32_16x16x32_bf16 v[60:63], v[146:149], v[178:181], v[60:63]
	v_mfma_f32_16x16x32_bf16 v[56:59], v[154:157], v[178:181], v[56:59]
	v_mfma_f32_16x16x32_bf16 v[52:55], v[146:149], v[186:189], v[52:55]
	v_mfma_f32_16x16x32_bf16 v[44:47], v[154:157], v[186:189], v[44:47]
	v_mfma_f32_16x16x32_bf16 v[36:39], v[146:149], v[198:201], v[36:39]
	v_mfma_f32_16x16x32_bf16 v[28:31], v[154:157], v[198:201], v[28:31]
	v_mfma_f32_16x16x32_bf16 v[20:23], v[146:149], v[206:209], v[20:23]
	v_mfma_f32_16x16x32_bf16 v[12:15], v[154:157], v[206:209], v[12:15]
	v_mfma_f32_16x16x32_bf16 v[60:63], v[150:153], v[182:185], v[60:63]
	v_mfma_f32_16x16x32_bf16 v[56:59], v[158:161], v[182:185], v[56:59]
	v_mfma_f32_16x16x32_bf16 v[52:55], v[150:153], v[190:193], v[52:55]
	v_mfma_f32_16x16x32_bf16 v[44:47], v[158:161], v[190:193], v[44:47]
	v_mfma_f32_16x16x32_bf16 v[36:39], v[150:153], v[202:205], v[36:39]
	v_mfma_f32_16x16x32_bf16 v[28:31], v[158:161], v[202:205], v[28:31]
	v_mfma_f32_16x16x32_bf16 v[20:23], v[150:153], v[210:213], v[20:23]
	v_mfma_f32_16x16x32_bf16 v[12:15], v[158:161], v[210:213], v[12:15]
	v_mfma_f32_16x16x32_bf16 v[48:51], v[162:165], v[178:181], v[48:51]
	v_mfma_f32_16x16x32_bf16 v[40:43], v[170:173], v[178:181], v[40:43]
	v_mfma_f32_16x16x32_bf16 v[32:35], v[162:165], v[186:189], v[32:35]
	v_mfma_f32_16x16x32_bf16 v[24:27], v[170:173], v[186:189], v[24:27]
	v_mfma_f32_16x16x32_bf16 v[16:19], v[162:165], v[198:201], v[16:19]
	v_mfma_f32_16x16x32_bf16 v[8:11], v[170:173], v[198:201], v[8:11]
	v_mfma_f32_16x16x32_bf16 v[4:7], v[162:165], v[206:209], v[4:7]
	v_mfma_f32_16x16x32_bf16 v[0:3], v[170:173], v[206:209], v[0:3]
	v_mfma_f32_16x16x32_bf16 v[48:51], v[166:169], v[182:185], v[48:51]
	v_mfma_f32_16x16x32_bf16 v[40:43], v[174:177], v[182:185], v[40:43]
	v_mfma_f32_16x16x32_bf16 v[32:35], v[166:169], v[190:193], v[32:35]
	v_mfma_f32_16x16x32_bf16 v[24:27], v[174:177], v[190:193], v[24:27]
	v_mfma_f32_16x16x32_bf16 v[16:19], v[166:169], v[202:205], v[16:19]
	v_mfma_f32_16x16x32_bf16 v[8:11], v[174:177], v[202:205], v[8:11]
	v_mfma_f32_16x16x32_bf16 v[4:7], v[166:169], v[210:213], v[4:7]
	v_mfma_f32_16x16x32_bf16 v[0:3], v[174:177], v[210:213], v[0:3]
	s_barrier
	s_add_i32 s66, s66, 2
	s_add_u32 s64, s64, 0x100
	s_addc_u32 s65, s65, 0
	s_add_u32 s15, s15, 0x100
	s_addc_u32 s17, s17, 0
	s_cmp_gt_u32 s66, 5
	s_cbranch_scc0 .LBB0_725
	s_and_b64 vcc, exec, s[10:11]
	s_cbranch_vccz .LBB0_728
	s_barrier

.LBB0_969:
	s_add_u32 s24, s18, s92
	s_addc_u32 s25, s19, s93
	s_add_u32 s60, s24, 0x100
	s_addc_u32 s61, s25, 0
	s_add_u32 s81, s2, s92
	s_addc_u32 s84, s29, s93
	s_add_i32 vcc_lo, 0, 0x10000
	s_cmpk_eq_i32 s92, 0xf00
	s_cselect_b64 s[26:27], -1, 0
	s_and_b64 s[24:25], s[26:27], exec
	s_cselect_b32 s25, s15, s61
	s_cselect_b32 s24, s17, s60
	s_waitcnt lgkmcnt(0)
	v_add_u32_e32 v104, vcc_lo, v234
	s_cselect_b32 s85, s67, s84
	s_cselect_b32 s84, s3, s81
	s_add_i32 s81, 0, 0x14000
	ds_read_b128 v[162:165], v104
	ds_read_b128 v[166:169], v104 offset:1024
	ds_read_b128 v[170:173], v104 offset:2048
	ds_read_b128 v[174:177], v104 offset:3072
	v_add_u32_e32 v104, s81, v234
	ds_read_b128 v[146:149], v104
	ds_read_b128 v[150:153], v104 offset:1024
	ds_read_b128 v[154:157], v104 offset:2048
	ds_read_b128 v[158:161], v104 offset:3072
	v_lshl_add_u64 v[104:105], v[208:209], 0, s[92:93]
	s_add_i32 m0, s53, 0xc000
	ds_read_b128 v[178:181], v236
	ds_read_b128 v[182:185], v236 offset:1024
	ds_read_b128 v[186:189], v236 offset:2048
	ds_read_b128 v[190:193], v236 offset:3072
	ds_read_b128 v[210:213], v236 offset:4096
	ds_read_b128 v[214:217], v236 offset:5120
	ds_read_b128 v[218:221], v236 offset:6144
	ds_read_b128 v[222:225], v236 offset:7168
	global_load_lds_dwordx4 v[104:105], off
	v_lshl_add_u64 v[104:105], v[206:207], 0, s[92:93]
	s_add_i32 m0, s53, 0xe000
	s_nop 0
	global_load_lds_dwordx4 v[104:105], off
	s_waitcnt vmcnt(8)
	s_waitcnt lgkmcnt(0)
	s_barrier
	v_mfma_f32_16x16x32_bf16 v[104:107], v[162:165], v[178:181], v[142:145]
	v_mfma_f32_16x16x32_bf16 v[108:111], v[170:173], v[178:181], v[138:141]
	v_mfma_f32_16x16x32_bf16 v[116:119], v[162:165], v[186:189], v[120:123]
	v_mfma_f32_16x16x32_bf16 v[112:115], v[170:173], v[186:189], v[112:115]
	v_mfma_f32_16x16x32_bf16 v[92:95], v[162:165], v[210:213], v[92:95]
	v_mfma_f32_16x16x32_bf16 v[88:91], v[170:173], v[210:213], v[88:91]
	v_mfma_f32_16x16x32_bf16 v[76:79], v[162:165], v[218:221], v[76:79]
	v_mfma_f32_16x16x32_bf16 v[72:75], v[170:173], v[218:221], v[72:75]
	v_mfma_f32_16x16x32_bf16 v[104:107], v[166:169], v[182:185], v[104:107]
	v_mfma_f32_16x16x32_bf16 v[108:111], v[174:177], v[182:185], v[108:111]
	v_mfma_f32_16x16x32_bf16 v[116:119], v[166:169], v[190:193], v[116:119]
	v_mfma_f32_16x16x32_bf16 v[112:115], v[174:177], v[190:193], v[112:115]
	v_mfma_f32_16x16x32_bf16 v[92:95], v[166:169], v[214:217], v[92:95]
	v_mfma_f32_16x16x32_bf16 v[88:91], v[174:177], v[214:217], v[88:91]
	v_mfma_f32_16x16x32_bf16 v[76:79], v[166:169], v[222:225], v[76:79]
	v_mfma_f32_16x16x32_bf16 v[72:75], v[174:177], v[222:225], v[72:75]
	v_mfma_f32_16x16x32_bf16 v[120:123], v[146:149], v[178:181], v[134:137]
	v_mfma_f32_16x16x32_bf16 v[130:133], v[150:153], v[182:185], v[120:123]
	v_mfma_f32_16x16x32_bf16 v[120:123], v[154:157], v[178:181], v[124:127]
	v_mfma_f32_16x16x32_bf16 v[100:103], v[146:149], v[186:189], v[100:103]
	v_mfma_f32_16x16x32_bf16 v[96:99], v[154:157], v[186:189], v[96:99]
	v_mfma_f32_16x16x32_bf16 v[84:87], v[146:149], v[210:213], v[84:87]
	v_mfma_f32_16x16x32_bf16 v[80:83], v[154:157], v[210:213], v[80:83]
	v_mfma_f32_16x16x32_bf16 v[68:71], v[146:149], v[218:221], v[68:71]
	v_mfma_f32_16x16x32_bf16 v[64:67], v[154:157], v[218:221], v[64:67]
	v_mfma_f32_16x16x32_bf16 v[124:127], v[158:161], v[182:185], v[120:123]
	v_mfma_f32_16x16x32_bf16 v[100:103], v[150:153], v[190:193], v[100:103]
	v_mfma_f32_16x16x32_bf16 v[96:99], v[158:161], v[190:193], v[96:99]
	v_mfma_f32_16x16x32_bf16 v[84:87], v[150:153], v[214:217], v[84:87]
	v_mfma_f32_16x16x32_bf16 v[80:83], v[158:161], v[214:217], v[80:83]
	v_mfma_f32_16x16x32_bf16 v[68:71], v[150:153], v[222:225], v[68:71]
	v_mfma_f32_16x16x32_bf16 v[64:67], v[158:161], v[222:225], v[64:67]
	s_barrier
	s_add_i32 s60, vcc_lo, s39
	v_lshl_add_u64 v[210:211], s[84:85], 0, v[198:199]
	s_mov_b32 m0, s60
	ds_read_b128 v[186:189], v236 offset:16384
	ds_read_b128 v[190:193], v236 offset:17408
	ds_read_b128 v[178:181], v236 offset:18432
	ds_read_b128 v[182:185], v236 offset:19456
	ds_read_b128 v[138:141], v236 offset:20480
	ds_read_b128 v[142:145], v236 offset:21504
	ds_read_b128 v[120:123], v236 offset:22528
	ds_read_b128 v[134:137], v236 offset:23552
	global_load_lds_dwordx4 v[210:211], off
	s_add_i32 m0, s60, 0x2000
	s_add_u32 s60, s84, 0x80000
	v_lshl_add_u64 v[212:213], s[84:85], 0, v[200:201]
	s_addc_u32 s61, s85, 0
	s_add_i32 s81, s81, s39
	global_load_lds_dwordx4 v[212:213], off
	s_mov_b32 m0, s81
	v_lshl_add_u64 v[216:217], s[24:25], 0, v[200:201]
	global_load_lds_dwordx4 v198, s[60:61]
	s_add_i32 m0, s81, 0x2000
	v_cndmask_b32_e64 v128, 0, 1, s[96:97]
	global_load_lds_dwordx4 v200, s[60:61]
	v_lshl_add_u64 v[214:215], s[24:25], 0, v[198:199]
	s_mov_b32 m0, s53
	v_cmp_ne_u32_e64 s[60:61], 1, v128
	global_load_lds_dwordx4 v[214:215], off
	s_mov_b32 m0, s88
	s_andn2_b64 vcc, exec, s[96:97]
	global_load_lds_dwordx4 v[216:217], off
	s_waitcnt vmcnt(8)
	s_waitcnt lgkmcnt(0)
	s_barrier
	s_cbranch_vccnz .LBB0_971
	s_waitcnt lgkmcnt(0)
	v_mfma_f32_16x16x32_bf16 v[60:63], v[162:165], v[186:189], v[60:63]
	v_mfma_f32_16x16x32_bf16 v[56:59], v[170:173], v[186:189], v[56:59]
	v_mfma_f32_16x16x32_bf16 v[44:47], v[162:165], v[178:181], v[44:47]
	v_mfma_f32_16x16x32_bf16 v[40:43], v[170:173], v[178:181], v[40:43]
	v_mfma_f32_16x16x32_bf16 v[28:31], v[162:165], v[138:141], v[28:31]
	v_mfma_f32_16x16x32_bf16 v[24:27], v[170:173], v[138:141], v[24:27]
	v_mfma_f32_16x16x32_bf16 v[12:15], v[162:165], v[120:123], v[12:15]
	v_mfma_f32_16x16x32_bf16 v[8:11], v[170:173], v[120:123], v[8:11]
	v_mfma_f32_16x16x32_bf16 v[60:63], v[166:169], v[190:193], v[60:63]
	v_mfma_f32_16x16x32_bf16 v[56:59], v[174:177], v[190:193], v[56:59]
	v_mfma_f32_16x16x32_bf16 v[44:47], v[166:169], v[182:185], v[44:47]
	v_mfma_f32_16x16x32_bf16 v[40:43], v[174:177], v[182:185], v[40:43]
	v_mfma_f32_16x16x32_bf16 v[28:31], v[166:169], v[142:145], v[28:31]
	v_mfma_f32_16x16x32_bf16 v[24:27], v[174:177], v[142:145], v[24:27]
	v_mfma_f32_16x16x32_bf16 v[12:15], v[166:169], v[134:137], v[12:15]
	v_mfma_f32_16x16x32_bf16 v[8:11], v[174:177], v[134:137], v[8:11]
	v_mfma_f32_16x16x32_bf16 v[52:55], v[146:149], v[186:189], v[52:55]
	v_mfma_f32_16x16x32_bf16 v[48:51], v[154:157], v[186:189], v[48:51]
	v_mfma_f32_16x16x32_bf16 v[36:39], v[146:149], v[178:181], v[36:39]
	v_mfma_f32_16x16x32_bf16 v[32:35], v[154:157], v[178:181], v[32:35]
	v_mfma_f32_16x16x32_bf16 v[20:23], v[146:149], v[138:141], v[20:23]
	v_mfma_f32_16x16x32_bf16 v[16:19], v[154:157], v[138:141], v[16:19]
	v_mfma_f32_16x16x32_bf16 v[4:7], v[146:149], v[120:123], v[4:7]
	v_mfma_f32_16x16x32_bf16 v[0:3], v[154:157], v[120:123], v[0:3]
	v_mfma_f32_16x16x32_bf16 v[52:55], v[150:153], v[190:193], v[52:55]
	v_mfma_f32_16x16x32_bf16 v[48:51], v[158:161], v[190:193], v[48:51]
	v_mfma_f32_16x16x32_bf16 v[36:39], v[150:153], v[182:185], v[36:39]
	v_mfma_f32_16x16x32_bf16 v[32:35], v[158:161], v[182:185], v[32:35]
	v_mfma_f32_16x16x32_bf16 v[20:23], v[150:153], v[142:145], v[20:23]
	v_mfma_f32_16x16x32_bf16 v[16:19], v[158:161], v[142:145], v[16:19]
	v_mfma_f32_16x16x32_bf16 v[4:7], v[150:153], v[134:137], v[4:7]
	v_mfma_f32_16x16x32_bf16 v[0:3], v[158:161], v[134:137], v[0:3]
.LBB0_971:
	s_barrier
	s_add_i32 s81, 0, 0x18000
	s_waitcnt lgkmcnt(0)
	v_add_u32_e32 v120, s81, v234
	s_add_i32 vcc_lo, 0, 0x1c000
	ds_read_b128 v[162:165], v120
	ds_read_b128 v[166:169], v120 offset:1024
	ds_read_b128 v[170:173], v120 offset:2048
	ds_read_b128 v[174:177], v120 offset:3072
	v_add_u32_e32 v120, vcc_lo, v234
	ds_read_b128 v[146:149], v120
	ds_read_b128 v[150:153], v120 offset:1024
	ds_read_b128 v[154:157], v120 offset:2048
	ds_read_b128 v[158:161], v120 offset:3072
	s_and_b64 s[26:27], s[26:27], exec
	s_cselect_b32 s27, s72, s20
	s_cselect_b32 s26, 0, s21
	s_add_u32 s24, s24, s27
	s_addc_u32 s25, s25, s26
	s_mov_b32 m0, s89
	ds_read_b128 v[178:181], v236 offset:32768
	ds_read_b128 v[182:185], v236 offset:33792
	ds_read_b128 v[186:189], v236 offset:34816
	ds_read_b128 v[190:193], v236 offset:35840
	ds_read_b128 v[218:221], v236 offset:36864
	ds_read_b128 v[222:225], v236 offset:37888
	ds_read_b128 v[226:229], v236 offset:38912
	ds_read_b128 v[238:241], v236 offset:39936
	global_load_lds_dwordx4 v198, s[24:25]
	v_lshl_add_u64 v[120:121], s[24:25], 0, v[200:201]
	s_mov_b32 m0, s90
	s_nop 0
	global_load_lds_dwordx4 v[120:121], off
	s_waitcnt vmcnt(8)
	s_waitcnt lgkmcnt(0)
	s_barrier
	v_mfma_f32_16x16x32_bf16 v[104:107], v[162:165], v[178:181], v[104:107]
	v_mfma_f32_16x16x32_bf16 v[142:145], v[166:169], v[182:185], v[104:107]
	v_mfma_f32_16x16x32_bf16 v[104:107], v[170:173], v[178:181], v[108:111]
	v_mfma_f32_16x16x32_bf16 v[138:141], v[174:177], v[182:185], v[104:107]
	v_mfma_f32_16x16x32_bf16 v[104:107], v[162:165], v[186:189], v[116:119]
	v_mfma_f32_16x16x32_bf16 v[120:123], v[166:169], v[190:193], v[104:107]
	v_mfma_f32_16x16x32_bf16 v[104:107], v[170:173], v[186:189], v[112:115]
	v_mfma_f32_16x16x32_bf16 v[92:95], v[162:165], v[218:221], v[92:95]
	v_mfma_f32_16x16x32_bf16 v[88:91], v[170:173], v[218:221], v[88:91]
	v_mfma_f32_16x16x32_bf16 v[76:79], v[162:165], v[226:229], v[76:79]
	v_mfma_f32_16x16x32_bf16 v[72:75], v[170:173], v[226:229], v[72:75]
	v_mfma_f32_16x16x32_bf16 v[112:115], v[174:177], v[190:193], v[104:107]
	v_mfma_f32_16x16x32_bf16 v[92:95], v[166:169], v[222:225], v[92:95]
	v_mfma_f32_16x16x32_bf16 v[88:91], v[174:177], v[222:225], v[88:91]
	v_mfma_f32_16x16x32_bf16 v[76:79], v[166:169], v[238:241], v[76:79]
	v_mfma_f32_16x16x32_bf16 v[72:75], v[174:177], v[238:241], v[72:75]
	v_mfma_f32_16x16x32_bf16 v[104:107], v[146:149], v[178:181], v[130:133]
	v_mfma_f32_16x16x32_bf16 v[134:137], v[150:153], v[182:185], v[104:107]
	v_mfma_f32_16x16x32_bf16 v[104:107], v[154:157], v[178:181], v[124:127]
	v_mfma_f32_16x16x32_bf16 v[100:103], v[146:149], v[186:189], v[100:103]
	v_mfma_f32_16x16x32_bf16 v[96:99], v[154:157], v[186:189], v[96:99]
	v_mfma_f32_16x16x32_bf16 v[84:87], v[146:149], v[218:221], v[84:87]
	v_mfma_f32_16x16x32_bf16 v[80:83], v[154:157], v[218:221], v[80:83]
	v_mfma_f32_16x16x32_bf16 v[68:71], v[146:149], v[226:229], v[68:71]
	v_mfma_f32_16x16x32_bf16 v[64:67], v[154:157], v[226:229], v[64:67]
	v_mfma_f32_16x16x32_bf16 v[124:127], v[158:161], v[182:185], v[104:107]
	v_mfma_f32_16x16x32_bf16 v[100:103], v[150:153], v[190:193], v[100:103]
	v_mfma_f32_16x16x32_bf16 v[96:99], v[158:161], v[190:193], v[96:99]
	v_mfma_f32_16x16x32_bf16 v[84:87], v[150:153], v[222:225], v[84:87]
	v_mfma_f32_16x16x32_bf16 v[80:83], v[158:161], v[222:225], v[80:83]
	v_mfma_f32_16x16x32_bf16 v[68:71], v[150:153], v[238:241], v[68:71]
	v_mfma_f32_16x16x32_bf16 v[64:67], v[158:161], v[238:241], v[64:67]
	s_barrier
	s_add_i32 s24, s81, s39
	v_lshl_add_u64 v[210:211], v[210:211], 0, s[42:43]
	s_mov_b32 m0, s24
	ds_read_b128 v[186:189], v236 offset:49152
	ds_read_b128 v[190:193], v236 offset:50176
	ds_read_b128 v[178:181], v236 offset:51200
	ds_read_b128 v[182:185], v236 offset:52224
	ds_read_b128 v[116:119], v236 offset:53248
	ds_read_b128 v[130:133], v236 offset:54272
	ds_read_b128 v[104:107], v236 offset:55296
	ds_read_b128 v[108:111], v236 offset:56320
	global_load_lds_dwordx4 v[210:211], off
	s_add_i32 m0, s24, 0x2000
	s_add_u32 s24, s84, 0x80080
	v_lshl_add_u64 v[210:211], v[212:213], 0, s[42:43]
	s_addc_u32 s25, s85, 0
	s_add_i32 s26, vcc_lo, s39
	global_load_lds_dwordx4 v[210:211], off
	s_mov_b32 m0, s26
	s_and_b64 vcc, exec, s[60:61]
	global_load_lds_dwordx4 v198, s[24:25]
	s_add_i32 m0, s26, 0x2000
	s_nop 0
	global_load_lds_dwordx4 v200, s[24:25]
	v_lshl_add_u64 v[210:211], v[214:215], 0, s[42:43]
	s_mov_b32 m0, s94
	s_nop 0
	global_load_lds_dwordx4 v[210:211], off
	v_lshl_add_u64 v[210:211], v[216:217], 0, s[42:43]
	s_mov_b32 m0, s33
	s_nop 0
	global_load_lds_dwordx4 v[210:211], off
	s_waitcnt vmcnt(8)
	s_waitcnt lgkmcnt(0)
	s_barrier
	s_cbranch_vccnz .LBB0_968
	s_waitcnt lgkmcnt(0)
	v_mfma_f32_16x16x32_bf16 v[60:63], v[162:165], v[186:189], v[60:63]
	v_mfma_f32_16x16x32_bf16 v[56:59], v[170:173], v[186:189], v[56:59]
	v_mfma_f32_16x16x32_bf16 v[44:47], v[162:165], v[178:181], v[44:47]
	v_mfma_f32_16x16x32_bf16 v[40:43], v[170:173], v[178:181], v[40:43]
	v_mfma_f32_16x16x32_bf16 v[28:31], v[162:165], v[116:119], v[28:31]
	v_mfma_f32_16x16x32_bf16 v[24:27], v[170:173], v[116:119], v[24:27]
	v_mfma_f32_16x16x32_bf16 v[12:15], v[162:165], v[104:107], v[12:15]
	v_mfma_f32_16x16x32_bf16 v[8:11], v[170:173], v[104:107], v[8:11]
	v_mfma_f32_16x16x32_bf16 v[60:63], v[166:169], v[190:193], v[60:63]
	v_mfma_f32_16x16x32_bf16 v[56:59], v[174:177], v[190:193], v[56:59]
	v_mfma_f32_16x16x32_bf16 v[44:47], v[166:169], v[182:185], v[44:47]
	v_mfma_f32_16x16x32_bf16 v[40:43], v[174:177], v[182:185], v[40:43]
	v_mfma_f32_16x16x32_bf16 v[28:31], v[166:169], v[130:133], v[28:31]
	v_mfma_f32_16x16x32_bf16 v[24:27], v[174:177], v[130:133], v[24:27]
	v_mfma_f32_16x16x32_bf16 v[12:15], v[166:169], v[108:111], v[12:15]
	v_mfma_f32_16x16x32_bf16 v[8:11], v[174:177], v[108:111], v[8:11]
	v_mfma_f32_16x16x32_bf16 v[52:55], v[146:149], v[186:189], v[52:55]
	v_mfma_f32_16x16x32_bf16 v[48:51], v[154:157], v[186:189], v[48:51]
	v_mfma_f32_16x16x32_bf16 v[36:39], v[146:149], v[178:181], v[36:39]
	v_mfma_f32_16x16x32_bf16 v[32:35], v[154:157], v[178:181], v[32:35]
	v_mfma_f32_16x16x32_bf16 v[20:23], v[146:149], v[116:119], v[20:23]
	v_mfma_f32_16x16x32_bf16 v[16:19], v[154:157], v[116:119], v[16:19]
	v_mfma_f32_16x16x32_bf16 v[4:7], v[146:149], v[104:107], v[4:7]
	v_mfma_f32_16x16x32_bf16 v[0:3], v[154:157], v[104:107], v[0:3]
	v_mfma_f32_16x16x32_bf16 v[52:55], v[150:153], v[190:193], v[52:55]
	v_mfma_f32_16x16x32_bf16 v[48:51], v[158:161], v[190:193], v[48:51]
	v_mfma_f32_16x16x32_bf16 v[36:39], v[150:153], v[182:185], v[36:39]
	v_mfma_f32_16x16x32_bf16 v[32:35], v[158:161], v[182:185], v[32:35]
	v_mfma_f32_16x16x32_bf16 v[20:23], v[150:153], v[130:133], v[20:23]
	v_mfma_f32_16x16x32_bf16 v[16:19], v[158:161], v[130:133], v[16:19]
	v_mfma_f32_16x16x32_bf16 v[4:7], v[150:153], v[108:111], v[4:7]
	v_mfma_f32_16x16x32_bf16 v[0:3], v[158:161], v[108:111], v[0:3]
	s_branch .LBB0_968

.LBB0_1443:
	s_lshl_b32 s72, s19, 7
	s_add_u32 s29, s76, s72
	s_addc_u32 s30, s77, 0
	s_add_u32 s22, s29, 0x100
	s_addc_u32 s23, s30, 0
	v_lshl_add_u64 v[144:145], v[142:143], 0, s[72:73]
	s_and_b64 s[2:3], s[60:61], exec
	v_lshl_add_u64 v[144:145], v[144:145], 0, s[46:47]
	s_cselect_b32 s23, s67, s23
	s_cselect_b32 s22, s66, s22
	v_cndmask_b32_e64 v145, v145, v141, s[60:61]
	v_cndmask_b32_e64 v144, v144, v140, s[60:61]
	s_add_i32 s60, 0, 0x10000
	v_add_u32_e32 v128, s60, v147
	s_add_i32 s61, 0, 0x14000
	ds_read_b128 v[150:153], v128
	ds_read_b128 v[154:157], v128 offset:1024
	ds_read_b128 v[158:161], v128 offset:2048
	ds_read_b128 v[162:165], v128 offset:3072
	v_add_u32_e32 v128, s61, v147
	ds_read_b128 v[166:169], v128
	ds_read_b128 v[170:173], v128 offset:1024
	ds_read_b128 v[174:177], v128 offset:2048
	ds_read_b128 v[178:181], v128 offset:3072
	s_add_u32 s2, s29, 0x20080
	s_addc_u32 s3, s30, 0
	s_add_i32 m0, s35, 0xc000
	ds_read_b128 v[182:185], v148
	ds_read_b128 v[186:189], v148 offset:1024
	ds_read_b128 v[190:193], v148 offset:2048
	ds_read_b128 v[198:201], v148 offset:3072
	ds_read_b128 v[202:205], v148 offset:4096
	ds_read_b128 v[206:209], v148 offset:5120
	ds_read_b128 v[210:213], v148 offset:6144
	ds_read_b128 v[214:217], v148 offset:7168
	global_load_lds_dwordx4 v130, s[2:3]
	s_add_i32 m0, s35, 0xe000
	s_nop 0
	global_load_lds_dwordx4 v134, s[2:3]
	s_waitcnt vmcnt(8)
	s_waitcnt lgkmcnt(0)
	s_barrier
	v_mfma_f32_16x16x32_bf16 v[124:127], v[150:153], v[182:185], v[124:127]
	v_mfma_f32_16x16x32_bf16 v[120:123], v[158:161], v[182:185], v[120:123]
	v_mfma_f32_16x16x32_bf16 v[112:115], v[150:153], v[190:193], v[112:115]
	v_mfma_f32_16x16x32_bf16 v[104:107], v[158:161], v[190:193], v[104:107]
	v_mfma_f32_16x16x32_bf16 v[96:99], v[150:153], v[202:205], v[96:99]
	v_mfma_f32_16x16x32_bf16 v[88:91], v[158:161], v[202:205], v[88:91]
	v_mfma_f32_16x16x32_bf16 v[80:83], v[150:153], v[210:213], v[80:83]
	v_mfma_f32_16x16x32_bf16 v[72:75], v[158:161], v[210:213], v[72:75]
	v_mfma_f32_16x16x32_bf16 v[124:127], v[154:157], v[186:189], v[124:127]
	v_mfma_f32_16x16x32_bf16 v[120:123], v[162:165], v[186:189], v[120:123]
	v_mfma_f32_16x16x32_bf16 v[112:115], v[154:157], v[198:201], v[112:115]
	v_mfma_f32_16x16x32_bf16 v[104:107], v[162:165], v[198:201], v[104:107]
	v_mfma_f32_16x16x32_bf16 v[96:99], v[154:157], v[206:209], v[96:99]
	v_mfma_f32_16x16x32_bf16 v[88:91], v[162:165], v[206:209], v[88:91]
	v_mfma_f32_16x16x32_bf16 v[80:83], v[154:157], v[214:217], v[80:83]
	v_mfma_f32_16x16x32_bf16 v[72:75], v[162:165], v[214:217], v[72:75]
	v_mfma_f32_16x16x32_bf16 v[116:119], v[166:169], v[182:185], v[116:119]
	v_mfma_f32_16x16x32_bf16 v[108:111], v[174:177], v[182:185], v[108:111]
	v_mfma_f32_16x16x32_bf16 v[100:103], v[166:169], v[190:193], v[100:103]
	v_mfma_f32_16x16x32_bf16 v[92:95], v[174:177], v[190:193], v[92:95]
	v_mfma_f32_16x16x32_bf16 v[84:87], v[166:169], v[202:205], v[84:87]
	v_mfma_f32_16x16x32_bf16 v[76:79], v[174:177], v[202:205], v[76:79]
	v_mfma_f32_16x16x32_bf16 v[68:71], v[166:169], v[210:213], v[68:71]
	v_mfma_f32_16x16x32_bf16 v[64:67], v[174:177], v[210:213], v[64:67]
	v_mfma_f32_16x16x32_bf16 v[116:119], v[170:173], v[186:189], v[116:119]
	v_mfma_f32_16x16x32_bf16 v[108:111], v[178:181], v[186:189], v[108:111]
	v_mfma_f32_16x16x32_bf16 v[100:103], v[170:173], v[198:201], v[100:103]
	v_mfma_f32_16x16x32_bf16 v[92:95], v[178:181], v[198:201], v[92:95]
	v_mfma_f32_16x16x32_bf16 v[84:87], v[170:173], v[206:209], v[84:87]
	v_mfma_f32_16x16x32_bf16 v[76:79], v[178:181], v[206:209], v[76:79]
	v_mfma_f32_16x16x32_bf16 v[68:71], v[170:173], v[214:217], v[68:71]
	v_mfma_f32_16x16x32_bf16 v[64:67], v[178:181], v[214:217], v[64:67]
	s_barrier
	s_add_i32 s2, s60, s33
	v_lshl_add_u64 v[194:195], v[144:145], 0, v[132:133]
	s_mov_b32 m0, s2
	ds_read_b128 v[182:185], v148 offset:16384
	ds_read_b128 v[186:189], v148 offset:17408
	ds_read_b128 v[190:193], v148 offset:18432
	ds_read_b128 v[198:201], v148 offset:19456
	ds_read_b128 v[202:205], v148 offset:20480
	ds_read_b128 v[206:209], v148 offset:21504
	ds_read_b128 v[210:213], v148 offset:22528
	ds_read_b128 v[214:217], v148 offset:23552
	global_load_lds_dwordx4 v[194:195], off
	v_lshl_add_u64 v[196:197], v[144:145], 0, v[136:137]
	s_add_i32 m0, s2, 0x2000
	v_lshl_add_u64 v[218:219], v[144:145], 0, s[48:49]
	s_add_i32 s2, s61, s33
	global_load_lds_dwordx4 v[196:197], off
	v_lshl_add_u64 v[220:221], v[218:219], 0, v[132:133]
	s_mov_b32 m0, s2
	v_lshl_add_u64 v[218:219], v[218:219], 0, v[136:137]
	global_load_lds_dwordx4 v[220:221], off
	s_add_i32 m0, s2, 0x2000
	v_lshl_add_u64 v[220:221], s[22:23], 0, v[134:135]
	global_load_lds_dwordx4 v[218:219], off
	v_lshl_add_u64 v[218:219], s[22:23], 0, v[130:131]
	s_mov_b32 m0, s35
	s_nop 0
	global_load_lds_dwordx4 v[218:219], off
	s_mov_b32 m0, s36
	s_nop 0
	global_load_lds_dwordx4 v[220:221], off
	s_waitcnt vmcnt(8)
	s_waitcnt lgkmcnt(0)
	s_barrier
	v_mfma_f32_16x16x32_bf16 v[60:63], v[150:153], v[182:185], v[60:63]
	v_mfma_f32_16x16x32_bf16 v[56:59], v[158:161], v[182:185], v[56:59]
	v_mfma_f32_16x16x32_bf16 v[48:51], v[150:153], v[190:193], v[48:51]
	v_mfma_f32_16x16x32_bf16 v[40:43], v[158:161], v[190:193], v[40:43]
	v_mfma_f32_16x16x32_bf16 v[32:35], v[150:153], v[202:205], v[32:35]
	v_mfma_f32_16x16x32_bf16 v[24:27], v[158:161], v[202:205], v[24:27]
	v_mfma_f32_16x16x32_bf16 v[16:19], v[150:153], v[210:213], v[16:19]
	v_mfma_f32_16x16x32_bf16 v[8:11], v[158:161], v[210:213], v[8:11]
	v_mfma_f32_16x16x32_bf16 v[60:63], v[154:157], v[186:189], v[60:63]
	v_mfma_f32_16x16x32_bf16 v[56:59], v[162:165], v[186:189], v[56:59]
	v_mfma_f32_16x16x32_bf16 v[48:51], v[154:157], v[198:201], v[48:51]
	v_mfma_f32_16x16x32_bf16 v[40:43], v[162:165], v[198:201], v[40:43]
	v_mfma_f32_16x16x32_bf16 v[32:35], v[154:157], v[206:209], v[32:35]
	v_mfma_f32_16x16x32_bf16 v[24:27], v[162:165], v[206:209], v[24:27]
	v_mfma_f32_16x16x32_bf16 v[16:19], v[154:157], v[214:217], v[16:19]
	v_mfma_f32_16x16x32_bf16 v[8:11], v[162:165], v[214:217], v[8:11]
	v_mfma_f32_16x16x32_bf16 v[52:55], v[166:169], v[182:185], v[52:55]
	v_mfma_f32_16x16x32_bf16 v[44:47], v[174:177], v[182:185], v[44:47]
	v_mfma_f32_16x16x32_bf16 v[36:39], v[166:169], v[190:193], v[36:39]
	v_mfma_f32_16x16x32_bf16 v[28:31], v[174:177], v[190:193], v[28:31]
	v_mfma_f32_16x16x32_bf16 v[20:23], v[166:169], v[202:205], v[20:23]
	v_mfma_f32_16x16x32_bf16 v[12:15], v[174:177], v[202:205], v[12:15]
	v_mfma_f32_16x16x32_bf16 v[4:7], v[166:169], v[210:213], v[4:7]
	v_mfma_f32_16x16x32_bf16 v[0:3], v[174:177], v[210:213], v[0:3]
	v_mfma_f32_16x16x32_bf16 v[52:55], v[170:173], v[186:189], v[52:55]
	v_mfma_f32_16x16x32_bf16 v[44:47], v[178:181], v[186:189], v[44:47]
	v_mfma_f32_16x16x32_bf16 v[36:39], v[170:173], v[198:201], v[36:39]
	v_mfma_f32_16x16x32_bf16 v[28:31], v[178:181], v[198:201], v[28:31]
	v_mfma_f32_16x16x32_bf16 v[20:23], v[170:173], v[206:209], v[20:23]
	v_mfma_f32_16x16x32_bf16 v[12:15], v[178:181], v[206:209], v[12:15]
	v_mfma_f32_16x16x32_bf16 v[4:7], v[170:173], v[214:217], v[4:7]
	v_mfma_f32_16x16x32_bf16 v[0:3], v[178:181], v[214:217], v[0:3]
	s_barrier
	s_add_i32 s29, 0, 0x18000
	v_add_u32_e32 v128, s29, v147
	s_add_i32 s30, 0, 0x1c000
	ds_read_b128 v[150:153], v128
	ds_read_b128 v[154:157], v128 offset:1024
	ds_read_b128 v[158:161], v128 offset:2048
	ds_read_b128 v[162:165], v128 offset:3072
	v_add_u32_e32 v128, s30, v147
	ds_read_b128 v[166:169], v128
	ds_read_b128 v[170:173], v128 offset:1024
	ds_read_b128 v[174:177], v128 offset:2048
	ds_read_b128 v[178:181], v128 offset:3072
	s_add_u32 s2, s22, 0x20000
	s_addc_u32 s3, s23, 0
	s_mov_b32 m0, s37
	ds_read_b128 v[182:185], v148 offset:32768
	ds_read_b128 v[186:189], v148 offset:33792
	ds_read_b128 v[190:193], v148 offset:34816
	ds_read_b128 v[198:201], v148 offset:35840
	ds_read_b128 v[202:205], v148 offset:36864
	ds_read_b128 v[206:209], v148 offset:37888
	ds_read_b128 v[210:213], v148 offset:38912
	ds_read_b128 v[214:217], v148 offset:39936
	global_load_lds_dwordx4 v130, s[2:3]
	s_mov_b32 m0, s38
	s_nop 0
	global_load_lds_dwordx4 v134, s[2:3]
	s_waitcnt vmcnt(8)
	s_waitcnt lgkmcnt(0)
	s_barrier
	v_mfma_f32_16x16x32_bf16 v[124:127], v[150:153], v[182:185], v[124:127]
	v_mfma_f32_16x16x32_bf16 v[120:123], v[158:161], v[182:185], v[120:123]
	v_mfma_f32_16x16x32_bf16 v[112:115], v[150:153], v[190:193], v[112:115]
	v_mfma_f32_16x16x32_bf16 v[104:107], v[158:161], v[190:193], v[104:107]
	v_mfma_f32_16x16x32_bf16 v[96:99], v[150:153], v[202:205], v[96:99]
	v_mfma_f32_16x16x32_bf16 v[88:91], v[158:161], v[202:205], v[88:91]
	v_mfma_f32_16x16x32_bf16 v[80:83], v[150:153], v[210:213], v[80:83]
	v_mfma_f32_16x16x32_bf16 v[72:75], v[158:161], v[210:213], v[72:75]
	v_mfma_f32_16x16x32_bf16 v[124:127], v[154:157], v[186:189], v[124:127]
	v_mfma_f32_16x16x32_bf16 v[120:123], v[162:165], v[186:189], v[120:123]
	v_mfma_f32_16x16x32_bf16 v[112:115], v[154:157], v[198:201], v[112:115]
	v_mfma_f32_16x16x32_bf16 v[104:107], v[162:165], v[198:201], v[104:107]
	v_mfma_f32_16x16x32_bf16 v[96:99], v[154:157], v[206:209], v[96:99]
	v_mfma_f32_16x16x32_bf16 v[88:91], v[162:165], v[206:209], v[88:91]
	v_mfma_f32_16x16x32_bf16 v[80:83], v[154:157], v[214:217], v[80:83]
	v_mfma_f32_16x16x32_bf16 v[72:75], v[162:165], v[214:217], v[72:75]
	v_mfma_f32_16x16x32_bf16 v[116:119], v[166:169], v[182:185], v[116:119]
	v_mfma_f32_16x16x32_bf16 v[108:111], v[174:177], v[182:185], v[108:111]
	v_mfma_f32_16x16x32_bf16 v[100:103], v[166:169], v[190:193], v[100:103]
	v_mfma_f32_16x16x32_bf16 v[92:95], v[174:177], v[190:193], v[92:95]
	v_mfma_f32_16x16x32_bf16 v[84:87], v[166:169], v[202:205], v[84:87]
	v_mfma_f32_16x16x32_bf16 v[76:79], v[174:177], v[202:205], v[76:79]
	v_mfma_f32_16x16x32_bf16 v[68:71], v[166:169], v[210:213], v[68:71]
	v_mfma_f32_16x16x32_bf16 v[64:67], v[174:177], v[210:213], v[64:67]
	v_mfma_f32_16x16x32_bf16 v[116:119], v[170:173], v[186:189], v[116:119]
	v_mfma_f32_16x16x32_bf16 v[108:111], v[178:181], v[186:189], v[108:111]
	v_mfma_f32_16x16x32_bf16 v[100:103], v[170:173], v[198:201], v[100:103]
	v_mfma_f32_16x16x32_bf16 v[92:95], v[178:181], v[198:201], v[92:95]
	v_mfma_f32_16x16x32_bf16 v[84:87], v[170:173], v[206:209], v[84:87]
	v_mfma_f32_16x16x32_bf16 v[76:79], v[178:181], v[206:209], v[76:79]
	v_mfma_f32_16x16x32_bf16 v[68:71], v[170:173], v[214:217], v[68:71]
	v_mfma_f32_16x16x32_bf16 v[64:67], v[178:181], v[214:217], v[64:67]
	s_barrier
	s_add_i32 s2, s29, s33
	v_lshl_add_u64 v[194:195], v[194:195], 0, s[42:43]
	s_mov_b32 m0, s2
	ds_read_b128 v[182:185], v148 offset:49152
	ds_read_b128 v[186:189], v148 offset:50176
	ds_read_b128 v[190:193], v148 offset:51200
	ds_read_b128 v[198:201], v148 offset:52224
	ds_read_b128 v[202:205], v148 offset:53248
	ds_read_b128 v[206:209], v148 offset:54272
	ds_read_b128 v[210:213], v148 offset:55296
	ds_read_b128 v[214:217], v148 offset:56320
	global_load_lds_dwordx4 v[194:195], off
	v_lshl_add_u64 v[194:195], v[196:197], 0, s[42:43]
	s_add_i32 m0, s2, 0x2000
	v_lshl_add_u64 v[144:145], v[144:145], 0, s[50:51]
	s_add_i32 s2, s30, s33
	global_load_lds_dwordx4 v[194:195], off
	v_lshl_add_u64 v[194:195], v[144:145], 0, v[132:133]
	s_mov_b32 m0, s2
	v_lshl_add_u64 v[144:145], v[144:145], 0, v[136:137]
	global_load_lds_dwordx4 v[194:195], off
	s_add_i32 m0, s2, 0x2000
	s_nop 0
	global_load_lds_dwordx4 v[144:145], off
	v_lshl_add_u64 v[144:145], v[218:219], 0, s[42:43]
	s_mov_b32 m0, s39
	s_nop 0
	global_load_lds_dwordx4 v[144:145], off
	v_lshl_add_u64 v[144:145], v[220:221], 0, s[42:43]
	s_mov_b32 m0, s53
	s_nop 0
	global_load_lds_dwordx4 v[144:145], off
	s_waitcnt vmcnt(8)
	s_waitcnt lgkmcnt(0)
	s_barrier
	v_mfma_f32_16x16x32_bf16 v[60:63], v[150:153], v[182:185], v[60:63]
	v_mfma_f32_16x16x32_bf16 v[56:59], v[158:161], v[182:185], v[56:59]
	v_mfma_f32_16x16x32_bf16 v[48:51], v[150:153], v[190:193], v[48:51]
	v_mfma_f32_16x16x32_bf16 v[40:43], v[158:161], v[190:193], v[40:43]
	v_mfma_f32_16x16x32_bf16 v[32:35], v[150:153], v[202:205], v[32:35]
	v_mfma_f32_16x16x32_bf16 v[24:27], v[158:161], v[202:205], v[24:27]
	v_mfma_f32_16x16x32_bf16 v[16:19], v[150:153], v[210:213], v[16:19]
	v_mfma_f32_16x16x32_bf16 v[8:11], v[158:161], v[210:213], v[8:11]
	v_mfma_f32_16x16x32_bf16 v[60:63], v[154:157], v[186:189], v[60:63]
	v_mfma_f32_16x16x32_bf16 v[56:59], v[162:165], v[186:189], v[56:59]
	v_mfma_f32_16x16x32_bf16 v[48:51], v[154:157], v[198:201], v[48:51]
	v_mfma_f32_16x16x32_bf16 v[40:43], v[162:165], v[198:201], v[40:43]
	v_mfma_f32_16x16x32_bf16 v[32:35], v[154:157], v[206:209], v[32:35]
	v_mfma_f32_16x16x32_bf16 v[24:27], v[162:165], v[206:209], v[24:27]
	v_mfma_f32_16x16x32_bf16 v[16:19], v[154:157], v[214:217], v[16:19]
	v_mfma_f32_16x16x32_bf16 v[8:11], v[162:165], v[214:217], v[8:11]
	v_mfma_f32_16x16x32_bf16 v[52:55], v[166:169], v[182:185], v[52:55]
	v_mfma_f32_16x16x32_bf16 v[44:47], v[174:177], v[182:185], v[44:47]
	v_mfma_f32_16x16x32_bf16 v[36:39], v[166:169], v[190:193], v[36:39]
	v_mfma_f32_16x16x32_bf16 v[28:31], v[174:177], v[190:193], v[28:31]
	v_mfma_f32_16x16x32_bf16 v[20:23], v[166:169], v[202:205], v[20:23]
	v_mfma_f32_16x16x32_bf16 v[12:15], v[174:177], v[202:205], v[12:15]
	v_mfma_f32_16x16x32_bf16 v[4:7], v[166:169], v[210:213], v[4:7]
	v_mfma_f32_16x16x32_bf16 v[0:3], v[174:177], v[210:213], v[0:3]
	v_mfma_f32_16x16x32_bf16 v[52:55], v[170:173], v[186:189], v[52:55]
	v_mfma_f32_16x16x32_bf16 v[44:47], v[178:181], v[186:189], v[44:47]
	v_mfma_f32_16x16x32_bf16 v[36:39], v[170:173], v[198:201], v[36:39]
	v_mfma_f32_16x16x32_bf16 v[28:31], v[178:181], v[198:201], v[28:31]
	v_mfma_f32_16x16x32_bf16 v[20:23], v[170:173], v[206:209], v[20:23]
	v_mfma_f32_16x16x32_bf16 v[12:15], v[178:181], v[206:209], v[12:15]
	v_mfma_f32_16x16x32_bf16 v[4:7], v[170:173], v[214:217], v[4:7]
	v_mfma_f32_16x16x32_bf16 v[0:3], v[178:181], v[214:217], v[0:3]
	s_barrier
	s_add_i32 s2, s19, 2
	s_cmp_gt_u32 s19, 5
	s_mov_b32 s19, s2
	s_cbranch_scc1 .LBB0_1450
